# v10 + MoE GEMM fp8 MFMAs in the unit-scale form without the scale-load half (v_mfma_f32_16x16x128_f8f6f4, same e4m3 operands and f32 accumulate; scales were the constant 1.0)
# speedup vs baseline: 1.0048x; 1.0048x over previous
.LBB0_832:
	s_add_u32 s44, s40, 0xed800100
	v_add_u32_e32 v1, s62, v158
	s_addc_u32 s45, s41, -1
	ds_read_b128 v[146:149], v1
	ds_read_b128 v[150:153], v1 offset:1024
	ds_read_b128 v[160:163], v1 offset:2048
	ds_read_b128 v[164:167], v1 offset:3072
	v_add_u32_e32 v1, s63, v158
	s_add_u32 s46, s18, s40
	ds_read_b128 v[168:171], v1
	ds_read_b128 v[172:175], v1 offset:1024
	ds_read_b128 v[176:179], v1 offset:2048
	ds_read_b128 v[180:183], v1 offset:3072
	s_addc_u32 s47, s19, s41
	s_add_u32 s46, s46, 0xed800100
	s_addc_u32 s47, s47, -1
	s_and_b64 s[42:43], s[42:43], exec
	s_cselect_b32 s42, s0, s46
	s_cselect_b32 s43, s1, s47
	s_cselect_b32 s69, s39, s45
	s_cselect_b32 s70, s38, s44
	s_add_u32 s44, s42, 0x80
	s_addc_u32 s45, s43, 0
	s_add_u32 s46, s90, s40
	s_addc_u32 s47, s91, s41
	s_add_u32 s46, s46, 0x80
	s_addc_u32 s47, s47, 0
	s_add_i32 m0, s7, 0xc000
	ds_read_b128 v[184:187], v143
	ds_read_b128 v[188:191], v143 offset:1024
	ds_read_b128 v[192:195], v143 offset:2048
	ds_read_b128 v[196:199], v143 offset:3072
	ds_read_b128 v[200:203], v143 offset:4096
	ds_read_b128 v[204:207], v143 offset:5120
	ds_read_b128 v[208:211], v143 offset:6144
	ds_read_b128 v[212:215], v143 offset:7168
	s_nop 0
	global_load_lds_dwordx4 v2, s[46:47]
	s_add_i32 m0, s7, 0xe000
	s_nop 0
	global_load_lds_dwordx4 v3, s[46:47]
	s_waitcnt vmcnt(8)
	s_waitcnt lgkmcnt(0)
	s_barrier
	s_setprio 1
	s_waitcnt lgkmcnt(0)
	v_mfma_f32_16x16x128_f8f6f4 v[128:131], v[146:153], v[184:191], v[128:131]
	v_mfma_f32_16x16x128_f8f6f4 v[124:127], v[160:167], v[184:191], v[124:127]
	v_mfma_f32_16x16x128_f8f6f4 v[120:123], v[146:153], v[192:199], v[120:123]
	v_mfma_f32_16x16x128_f8f6f4 v[116:119], v[160:167], v[192:199], v[116:119]
	v_mfma_f32_16x16x128_f8f6f4 v[112:115], v[146:153], v[200:207], v[112:115]
	v_mfma_f32_16x16x128_f8f6f4 v[108:111], v[160:167], v[200:207], v[108:111]
	v_mfma_f32_16x16x128_f8f6f4 v[104:107], v[146:153], v[208:215], v[104:107]
	v_mfma_f32_16x16x128_f8f6f4 v[100:103], v[160:167], v[208:215], v[100:103]
	s_setprio 0
	s_setprio 1
	v_mfma_f32_16x16x128_f8f6f4 v[136:139], v[168:175], v[184:191], v[96:99]
	v_mfma_f32_16x16x128_f8f6f4 v[184:187], v[176:183], v[184:191], v[92:95]
	v_mfma_f32_16x16x128_f8f6f4 v[188:191], v[168:175], v[192:199], v[88:91]
	v_mfma_f32_16x16x128_f8f6f4 v[192:195], v[176:183], v[192:199], v[84:87]
	v_mfma_f32_16x16x128_f8f6f4 v[196:199], v[168:175], v[200:207], v[80:83]
	v_mfma_f32_16x16x128_f8f6f4 v[200:203], v[176:183], v[200:207], v[76:79]
	v_mfma_f32_16x16x128_f8f6f4 v[204:207], v[168:175], v[208:215], v[72:75]
	v_mfma_f32_16x16x128_f8f6f4 v[208:211], v[176:183], v[208:215], v[28:31]
	s_setprio 0
	s_barrier
	s_add_i32 s71, s62, s52
	s_mov_b64 s[46:47], s[42:43]
	s_mov_b32 m0, s71
	ds_read_b128 v[68:71], v143 offset:16384
	ds_read_b128 v[72:75], v143 offset:17408
	ds_read_b128 v[76:79], v143 offset:18432
	ds_read_b128 v[80:83], v143 offset:19456
	ds_read_b128 v[84:87], v143 offset:20480
	ds_read_b128 v[88:91], v143 offset:21504
	ds_read_b128 v[92:95], v143 offset:22528
	ds_read_b128 v[96:99], v143 offset:23552
	s_nop 0
	global_load_lds_dwordx4 v140, s[46:47]
	s_add_i32 m0, s71, 0x2000
	s_nop 0
	global_load_lds_dwordx4 v142, s[46:47]
	s_add_u32 s46, s42, 0x40000
	s_addc_u32 s47, s43, 0
	s_add_i32 s71, s63, s52
	s_mov_b32 m0, s71
	s_nop 0
	global_load_lds_dwordx4 v140, s[46:47]
	s_add_i32 m0, s71, 0x2000
	s_nop 0
	global_load_lds_dwordx4 v142, s[46:47]
	s_add_u32 s46, s16, s70
	s_addc_u32 s47, s17, s69
	s_mov_b64 s[70:71], s[46:47]
	s_mov_b32 m0, s7
	s_nop 0
	global_load_lds_dwordx4 v132, s[70:71]
	s_mov_b32 m0, s25
	s_nop 0
	global_load_lds_dwordx4 v133, s[70:71]
	s_waitcnt vmcnt(8)
	s_waitcnt lgkmcnt(0)
	s_barrier
	s_setprio 1
	s_waitcnt lgkmcnt(0)
	v_mfma_f32_16x16x128_f8f6f4 v[64:67], v[146:153], v[68:75], v[64:67]
	v_mfma_f32_16x16x128_f8f6f4 v[60:63], v[160:167], v[68:75], v[60:63]
	v_mfma_f32_16x16x128_f8f6f4 v[56:59], v[146:153], v[76:83], v[56:59]
	v_mfma_f32_16x16x128_f8f6f4 v[52:55], v[160:167], v[76:83], v[52:55]
	v_mfma_f32_16x16x128_f8f6f4 v[212:215], v[146:153], v[84:91], v[48:51]
	v_mfma_f32_16x16x128_f8f6f4 v[216:219], v[160:167], v[84:91], v[44:47]
	v_mfma_f32_16x16x128_f8f6f4 v[220:223], v[146:153], v[92:99], v[40:43]
	v_mfma_f32_16x16x128_f8f6f4 v[224:227], v[160:167], v[92:99], v[36:39]
	s_setprio 0
	s_setprio 1
	v_mfma_f32_16x16x128_f8f6f4 v[232:235], v[176:183], v[68:75], v[232:235]
	v_mfma_f32_16x16x128_f8f6f4 v[228:231], v[168:175], v[68:75], v[32:35]
	v_mfma_f32_16x16x128_f8f6f4 v[236:239], v[168:175], v[76:83], v[24:27]
	v_mfma_f32_16x16x128_f8f6f4 v[240:243], v[176:183], v[76:83], v[20:23]
	v_mfma_f32_16x16x128_f8f6f4 v[244:247], v[168:175], v[84:91], v[16:19]
	v_mfma_f32_16x16x128_f8f6f4 v[248:251], v[176:183], v[84:91], v[12:15]
	v_mfma_f32_16x16x128_f8f6f4 v[154:157], v[168:175], v[92:99], v[8:11]
	v_mfma_f32_16x16x128_f8f6f4 v[68:71], v[176:183], v[92:99], v[4:7]
	s_setprio 0
	s_barrier
	s_add_i32 s69, 0, 0x18000
	v_add_u32_e32 v1, s69, v158
	s_add_i32 s72, 0, 0x1c000
	s_nop 1
	ds_read_b128 v[4:7], v1
	ds_read_b128 v[8:11], v1 offset:1024
	ds_read_b128 v[12:15], v1 offset:2048
	ds_read_b128 v[16:19], v1 offset:3072
	v_add_u32_e32 v1, s72, v158
	ds_read_b128 v[146:149], v1
	ds_read_b128 v[150:153], v1 offset:1024
	ds_read_b128 v[160:163], v1 offset:2048
	ds_read_b128 v[164:167], v1 offset:3072
	s_mov_b64 s[70:71], s[46:47]
	s_mov_b32 m0, s33
	ds_read_b128 v[20:23], v143 offset:32768
	ds_read_b128 v[24:27], v143 offset:33792
	ds_read_b128 v[28:31], v143 offset:34816
	ds_read_b128 v[32:35], v143 offset:35840
	ds_read_b128 v[36:39], v143 offset:36864
	ds_read_b128 v[40:43], v143 offset:37888
	ds_read_b128 v[44:47], v143 offset:38912
	ds_read_b128 v[48:51], v143 offset:39936
	s_nop 0
	global_load_lds_dwordx4 v134, s[70:71]
	s_mov_b32 m0, s58
	s_nop 0
	global_load_lds_dwordx4 v135, s[70:71]
	s_waitcnt vmcnt(8)
	s_waitcnt lgkmcnt(0)
	s_barrier
	s_setprio 1
	s_waitcnt lgkmcnt(0)
	v_mfma_f32_16x16x128_f8f6f4 v[128:131], v[4:11], v[20:27], v[128:131]
	v_mfma_f32_16x16x128_f8f6f4 v[124:127], v[12:19], v[20:27], v[124:127]
	v_mfma_f32_16x16x128_f8f6f4 v[120:123], v[4:11], v[28:35], v[120:123]
	v_mfma_f32_16x16x128_f8f6f4 v[116:119], v[12:19], v[28:35], v[116:119]
	v_mfma_f32_16x16x128_f8f6f4 v[112:115], v[4:11], v[36:43], v[112:115]
	v_mfma_f32_16x16x128_f8f6f4 v[108:111], v[12:19], v[36:43], v[108:111]
	v_mfma_f32_16x16x128_f8f6f4 v[104:107], v[4:11], v[44:51], v[104:107]
	v_mfma_f32_16x16x128_f8f6f4 v[100:103], v[12:19], v[44:51], v[100:103]
	s_setprio 0
	s_setprio 1
	v_mfma_f32_16x16x128_f8f6f4 v[96:99], v[146:153], v[20:27], v[136:139]
	v_mfma_f32_16x16x128_f8f6f4 v[92:95], v[160:167], v[20:27], v[184:187]
	v_mfma_f32_16x16x128_f8f6f4 v[88:91], v[146:153], v[28:35], v[188:191]
	v_mfma_f32_16x16x128_f8f6f4 v[84:87], v[160:167], v[28:35], v[192:195]
	v_mfma_f32_16x16x128_f8f6f4 v[80:83], v[146:153], v[36:43], v[196:199]
	v_mfma_f32_16x16x128_f8f6f4 v[76:79], v[160:167], v[36:43], v[200:203]
	v_mfma_f32_16x16x128_f8f6f4 v[72:75], v[146:153], v[44:51], v[204:207]
	v_mfma_f32_16x16x128_f8f6f4 v[28:31], v[160:167], v[44:51], v[208:211]
	s_setprio 0
	s_barrier
	s_add_i32 s69, s69, s52
	s_mov_b32 m0, s69
	ds_read_b128 v[20:23], v143 offset:49152
	ds_read_b128 v[24:27], v143 offset:50176
	ds_read_b128 v[168:171], v143 offset:51200
	ds_read_b128 v[172:175], v143 offset:52224
	ds_read_b128 v[176:179], v143 offset:53248
	ds_read_b128 v[180:183], v143 offset:54272
	ds_read_b128 v[184:187], v143 offset:55296
	ds_read_b128 v[188:191], v143 offset:56320
	s_nop 0
	global_load_lds_dwordx4 v140, s[44:45]
	s_add_i32 m0, s69, 0x2000
	s_add_u32 s42, s42, 0x40080
	global_load_lds_dwordx4 v142, s[44:45]
	s_addc_u32 s43, s43, 0
	s_add_i32 s44, s72, s52
	s_mov_b32 m0, s44
	s_nop 0
	global_load_lds_dwordx4 v140, s[42:43]
	s_add_i32 m0, s44, 0x2000
	s_nop 0
	global_load_lds_dwordx4 v142, s[42:43]
	s_add_u32 s42, s46, 0x80
	s_addc_u32 s43, s47, 0
	s_mov_b32 m0, s60
	s_nop 0
	global_load_lds_dwordx4 v132, s[42:43]
	s_mov_b32 m0, s61
	s_nop 0
	global_load_lds_dwordx4 v133, s[42:43]
	s_waitcnt vmcnt(8)
	s_waitcnt lgkmcnt(0)
	s_barrier
	s_setprio 1
	s_waitcnt lgkmcnt(0)
	v_mfma_f32_16x16x128_f8f6f4 v[64:67], v[4:11], v[20:27], v[64:67]
	v_mfma_f32_16x16x128_f8f6f4 v[60:63], v[12:19], v[20:27], v[60:63]
	v_mfma_f32_16x16x128_f8f6f4 v[56:59], v[4:11], v[168:175], v[56:59]
	v_mfma_f32_16x16x128_f8f6f4 v[52:55], v[12:19], v[168:175], v[52:55]
	v_mfma_f32_16x16x128_f8f6f4 v[48:51], v[4:11], v[176:183], v[212:215]
	v_mfma_f32_16x16x128_f8f6f4 v[44:47], v[12:19], v[176:183], v[216:219]
	v_mfma_f32_16x16x128_f8f6f4 v[40:43], v[4:11], v[184:191], v[220:223]
	v_mfma_f32_16x16x128_f8f6f4 v[36:39], v[12:19], v[184:191], v[224:227]
	s_setprio 0
	s_setprio 1
	v_mfma_f32_16x16x128_f8f6f4 v[32:35], v[146:153], v[20:27], v[228:231]
	v_mfma_f32_16x16x128_f8f6f4 v[232:235], v[160:167], v[20:27], v[232:235]
	v_mfma_f32_16x16x128_f8f6f4 v[24:27], v[146:153], v[168:175], v[236:239]
	v_mfma_f32_16x16x128_f8f6f4 v[20:23], v[160:167], v[168:175], v[240:243]
	v_mfma_f32_16x16x128_f8f6f4 v[16:19], v[146:153], v[176:183], v[244:247]
	v_mfma_f32_16x16x128_f8f6f4 v[12:15], v[160:167], v[176:183], v[248:251]
	v_mfma_f32_16x16x128_f8f6f4 v[8:11], v[146:153], v[184:191], v[154:157]
	v_mfma_f32_16x16x128_f8f6f4 v[4:7], v[160:167], v[184:191], v[68:71]
	s_setprio 0
	s_barrier
	s_add_i32 s5, s5, 2
	s_add_u32 s40, s40, 0x100
	s_addc_u32 s41, s41, 0
	s_cmp_gt_u32 s5, 13
	s_cbranch_scc1 .LBB0_835

.LBB0_917:
	s_add_u32 s44, s40, 0xed800100
	v_add_u32_e32 v1, s57, v158
	s_addc_u32 s45, s41, -1
	ds_read_b128 v[146:149], v1
	ds_read_b128 v[150:153], v1 offset:1024
	ds_read_b128 v[160:163], v1 offset:2048
	ds_read_b128 v[164:167], v1 offset:3072
	v_add_u32_e32 v1, s61, v158
	s_add_u32 s46, s18, s40
	ds_read_b128 v[168:171], v1
	ds_read_b128 v[172:175], v1 offset:1024
	ds_read_b128 v[176:179], v1 offset:2048
	ds_read_b128 v[180:183], v1 offset:3072
	s_addc_u32 s47, s19, s41
	s_add_u32 s46, s46, 0xed800100
	s_addc_u32 s47, s47, -1
	s_and_b64 s[42:43], s[42:43], exec
	s_cselect_b32 s42, s0, s46
	s_cselect_b32 s43, s1, s47
	s_cselect_b32 s68, s39, s45
	s_cselect_b32 s69, s38, s44
	s_add_u32 s44, s42, 0x80
	s_addc_u32 s45, s43, 0
	s_add_u32 s46, s90, s40
	s_addc_u32 s47, s91, s41
	s_add_u32 s46, s46, 0x80
	s_addc_u32 s47, s47, 0
	s_add_i32 m0, s7, 0xc000
	ds_read_b128 v[184:187], v143
	ds_read_b128 v[188:191], v143 offset:1024
	ds_read_b128 v[192:195], v143 offset:2048
	ds_read_b128 v[196:199], v143 offset:3072
	ds_read_b128 v[200:203], v143 offset:4096
	ds_read_b128 v[204:207], v143 offset:5120
	ds_read_b128 v[208:211], v143 offset:6144
	ds_read_b128 v[212:215], v143 offset:7168
	s_nop 0
	global_load_lds_dwordx4 v2, s[46:47]
	s_add_i32 m0, s7, 0xe000
	s_nop 0
	global_load_lds_dwordx4 v3, s[46:47]
	s_waitcnt vmcnt(8)
	s_waitcnt lgkmcnt(0)
	s_barrier
	s_setprio 1
	s_waitcnt lgkmcnt(0)
	v_mfma_f32_16x16x128_f8f6f4 v[128:131], v[146:153], v[184:191], v[128:131]
	v_mfma_f32_16x16x128_f8f6f4 v[124:127], v[160:167], v[184:191], v[124:127]
	v_mfma_f32_16x16x128_f8f6f4 v[120:123], v[146:153], v[192:199], v[120:123]
	v_mfma_f32_16x16x128_f8f6f4 v[116:119], v[160:167], v[192:199], v[116:119]
	v_mfma_f32_16x16x128_f8f6f4 v[112:115], v[146:153], v[200:207], v[112:115]
	v_mfma_f32_16x16x128_f8f6f4 v[108:111], v[160:167], v[200:207], v[108:111]
	v_mfma_f32_16x16x128_f8f6f4 v[104:107], v[146:153], v[208:215], v[104:107]
	v_mfma_f32_16x16x128_f8f6f4 v[100:103], v[160:167], v[208:215], v[100:103]
	s_setprio 0
	s_setprio 1
	v_mfma_f32_16x16x128_f8f6f4 v[136:139], v[168:175], v[184:191], v[96:99]
	v_mfma_f32_16x16x128_f8f6f4 v[184:187], v[176:183], v[184:191], v[92:95]
	v_mfma_f32_16x16x128_f8f6f4 v[188:191], v[168:175], v[192:199], v[88:91]
	v_mfma_f32_16x16x128_f8f6f4 v[192:195], v[176:183], v[192:199], v[84:87]
	v_mfma_f32_16x16x128_f8f6f4 v[196:199], v[168:175], v[200:207], v[80:83]
	v_mfma_f32_16x16x128_f8f6f4 v[200:203], v[176:183], v[200:207], v[76:79]
	v_mfma_f32_16x16x128_f8f6f4 v[204:207], v[168:175], v[208:215], v[72:75]
	v_mfma_f32_16x16x128_f8f6f4 v[208:211], v[176:183], v[208:215], v[28:31]
	s_setprio 0
	s_barrier
	s_add_i32 s70, s57, s52
	s_mov_b64 s[46:47], s[42:43]
	s_mov_b32 m0, s70
	ds_read_b128 v[68:71], v143 offset:16384
	ds_read_b128 v[72:75], v143 offset:17408
	ds_read_b128 v[76:79], v143 offset:18432
	ds_read_b128 v[80:83], v143 offset:19456
	ds_read_b128 v[84:87], v143 offset:20480
	ds_read_b128 v[88:91], v143 offset:21504
	ds_read_b128 v[92:95], v143 offset:22528
	ds_read_b128 v[96:99], v143 offset:23552
	s_nop 0
	global_load_lds_dwordx4 v140, s[46:47]
	s_add_i32 m0, s70, 0x2000
	s_nop 0
	global_load_lds_dwordx4 v142, s[46:47]
	s_add_u32 s46, s42, 0x40000
	s_addc_u32 s47, s43, 0
	s_add_i32 s70, s61, s52
	s_mov_b32 m0, s70
	s_nop 0
	global_load_lds_dwordx4 v140, s[46:47]
	s_add_i32 m0, s70, 0x2000
	s_nop 0
	global_load_lds_dwordx4 v142, s[46:47]
	s_add_u32 s46, s16, s69
	s_addc_u32 s47, s17, s68
	s_mov_b64 s[68:69], s[46:47]
	s_mov_b32 m0, s7
	s_nop 0
	global_load_lds_dwordx4 v132, s[68:69]
	s_mov_b32 m0, s25
	s_nop 0
	global_load_lds_dwordx4 v133, s[68:69]
	s_waitcnt vmcnt(8)
	s_waitcnt lgkmcnt(0)
	s_barrier
	s_setprio 1
	s_waitcnt lgkmcnt(0)
	v_mfma_f32_16x16x128_f8f6f4 v[64:67], v[146:153], v[68:75], v[64:67]
	v_mfma_f32_16x16x128_f8f6f4 v[60:63], v[160:167], v[68:75], v[60:63]
	v_mfma_f32_16x16x128_f8f6f4 v[56:59], v[146:153], v[76:83], v[56:59]
	v_mfma_f32_16x16x128_f8f6f4 v[52:55], v[160:167], v[76:83], v[52:55]
	v_mfma_f32_16x16x128_f8f6f4 v[212:215], v[146:153], v[84:91], v[48:51]
	v_mfma_f32_16x16x128_f8f6f4 v[216:219], v[160:167], v[84:91], v[44:47]
	v_mfma_f32_16x16x128_f8f6f4 v[220:223], v[146:153], v[92:99], v[40:43]
	v_mfma_f32_16x16x128_f8f6f4 v[224:227], v[160:167], v[92:99], v[36:39]
	s_setprio 0
	s_setprio 1
	v_mfma_f32_16x16x128_f8f6f4 v[232:235], v[176:183], v[68:75], v[232:235]
	v_mfma_f32_16x16x128_f8f6f4 v[228:231], v[168:175], v[68:75], v[32:35]
	v_mfma_f32_16x16x128_f8f6f4 v[236:239], v[168:175], v[76:83], v[24:27]
	v_mfma_f32_16x16x128_f8f6f4 v[240:243], v[176:183], v[76:83], v[20:23]
	v_mfma_f32_16x16x128_f8f6f4 v[244:247], v[168:175], v[84:91], v[16:19]
	v_mfma_f32_16x16x128_f8f6f4 v[248:251], v[176:183], v[84:91], v[12:15]
	v_mfma_f32_16x16x128_f8f6f4 v[154:157], v[168:175], v[92:99], v[8:11]
	v_mfma_f32_16x16x128_f8f6f4 v[68:71], v[176:183], v[92:99], v[4:7]
	s_setprio 0
	s_barrier
	s_add_i32 s70, 0, 0x18000
	v_add_u32_e32 v1, s70, v158
	s_add_i32 s71, 0, 0x1c000
	s_nop 1
	ds_read_b128 v[4:7], v1
	ds_read_b128 v[8:11], v1 offset:1024
	ds_read_b128 v[12:15], v1 offset:2048
	ds_read_b128 v[16:19], v1 offset:3072
	v_add_u32_e32 v1, s71, v158
	ds_read_b128 v[146:149], v1
	ds_read_b128 v[150:153], v1 offset:1024
	ds_read_b128 v[160:163], v1 offset:2048
	ds_read_b128 v[164:167], v1 offset:3072
	s_mov_b64 s[68:69], s[46:47]
	s_mov_b32 m0, s33
	ds_read_b128 v[20:23], v143 offset:32768
	ds_read_b128 v[24:27], v143 offset:33792
	ds_read_b128 v[28:31], v143 offset:34816
	ds_read_b128 v[32:35], v143 offset:35840
	ds_read_b128 v[36:39], v143 offset:36864
	ds_read_b128 v[40:43], v143 offset:37888
	ds_read_b128 v[44:47], v143 offset:38912
	ds_read_b128 v[48:51], v143 offset:39936
	s_nop 0
	global_load_lds_dwordx4 v134, s[68:69]
	s_mov_b32 m0, s58
	s_nop 0
	global_load_lds_dwordx4 v135, s[68:69]
	s_waitcnt vmcnt(8)
	s_waitcnt lgkmcnt(0)
	s_barrier
	s_setprio 1
	s_waitcnt lgkmcnt(0)
	v_mfma_f32_16x16x128_f8f6f4 v[128:131], v[4:11], v[20:27], v[128:131]
	v_mfma_f32_16x16x128_f8f6f4 v[124:127], v[12:19], v[20:27], v[124:127]
	v_mfma_f32_16x16x128_f8f6f4 v[120:123], v[4:11], v[28:35], v[120:123]
	v_mfma_f32_16x16x128_f8f6f4 v[116:119], v[12:19], v[28:35], v[116:119]
	v_mfma_f32_16x16x128_f8f6f4 v[112:115], v[4:11], v[36:43], v[112:115]
	v_mfma_f32_16x16x128_f8f6f4 v[108:111], v[12:19], v[36:43], v[108:111]
	v_mfma_f32_16x16x128_f8f6f4 v[104:107], v[4:11], v[44:51], v[104:107]
	v_mfma_f32_16x16x128_f8f6f4 v[100:103], v[12:19], v[44:51], v[100:103]
	s_setprio 0
	s_setprio 1
	v_mfma_f32_16x16x128_f8f6f4 v[96:99], v[146:153], v[20:27], v[136:139]
	v_mfma_f32_16x16x128_f8f6f4 v[92:95], v[160:167], v[20:27], v[184:187]
	v_mfma_f32_16x16x128_f8f6f4 v[88:91], v[146:153], v[28:35], v[188:191]
	v_mfma_f32_16x16x128_f8f6f4 v[84:87], v[160:167], v[28:35], v[192:195]
	v_mfma_f32_16x16x128_f8f6f4 v[80:83], v[146:153], v[36:43], v[196:199]
	v_mfma_f32_16x16x128_f8f6f4 v[76:79], v[160:167], v[36:43], v[200:203]
	v_mfma_f32_16x16x128_f8f6f4 v[72:75], v[146:153], v[44:51], v[204:207]
	v_mfma_f32_16x16x128_f8f6f4 v[28:31], v[160:167], v[44:51], v[208:211]
	s_setprio 0
	s_barrier
	s_add_i32 s68, s70, s52
	s_mov_b32 m0, s68
	ds_read_b128 v[20:23], v143 offset:49152
	ds_read_b128 v[24:27], v143 offset:50176
	ds_read_b128 v[168:171], v143 offset:51200
	ds_read_b128 v[172:175], v143 offset:52224
	ds_read_b128 v[176:179], v143 offset:53248
	ds_read_b128 v[180:183], v143 offset:54272
	ds_read_b128 v[184:187], v143 offset:55296
	ds_read_b128 v[188:191], v143 offset:56320
	s_nop 0
	global_load_lds_dwordx4 v140, s[44:45]
	s_add_i32 m0, s68, 0x2000
	s_add_u32 s42, s42, 0x40080
	global_load_lds_dwordx4 v142, s[44:45]
	s_addc_u32 s43, s43, 0
	s_add_i32 s44, s71, s52
	s_mov_b32 m0, s44
	s_nop 0
	global_load_lds_dwordx4 v140, s[42:43]
	s_add_i32 m0, s44, 0x2000
	s_nop 0
	global_load_lds_dwordx4 v142, s[42:43]
	s_add_u32 s42, s46, 0x80
	s_addc_u32 s43, s47, 0
	s_mov_b32 m0, s55
	s_nop 0
	global_load_lds_dwordx4 v132, s[42:43]
	s_mov_b32 m0, s56
	s_nop 0
	global_load_lds_dwordx4 v133, s[42:43]
	s_waitcnt vmcnt(8)
	s_waitcnt lgkmcnt(0)
	s_barrier
	s_setprio 1
	s_waitcnt lgkmcnt(0)
	v_mfma_f32_16x16x128_f8f6f4 v[64:67], v[4:11], v[20:27], v[64:67]
	v_mfma_f32_16x16x128_f8f6f4 v[60:63], v[12:19], v[20:27], v[60:63]
	v_mfma_f32_16x16x128_f8f6f4 v[56:59], v[4:11], v[168:175], v[56:59]
	v_mfma_f32_16x16x128_f8f6f4 v[52:55], v[12:19], v[168:175], v[52:55]
	v_mfma_f32_16x16x128_f8f6f4 v[48:51], v[4:11], v[176:183], v[212:215]
	v_mfma_f32_16x16x128_f8f6f4 v[44:47], v[12:19], v[176:183], v[216:219]
	v_mfma_f32_16x16x128_f8f6f4 v[40:43], v[4:11], v[184:191], v[220:223]
	v_mfma_f32_16x16x128_f8f6f4 v[36:39], v[12:19], v[184:191], v[224:227]
	s_setprio 0
	s_setprio 1
	v_mfma_f32_16x16x128_f8f6f4 v[32:35], v[146:153], v[20:27], v[228:231]
	v_mfma_f32_16x16x128_f8f6f4 v[232:235], v[160:167], v[20:27], v[232:235]
	v_mfma_f32_16x16x128_f8f6f4 v[24:27], v[146:153], v[168:175], v[236:239]
	v_mfma_f32_16x16x128_f8f6f4 v[20:23], v[160:167], v[168:175], v[240:243]
	v_mfma_f32_16x16x128_f8f6f4 v[16:19], v[146:153], v[176:183], v[244:247]
	v_mfma_f32_16x16x128_f8f6f4 v[12:15], v[160:167], v[176:183], v[248:251]
	v_mfma_f32_16x16x128_f8f6f4 v[8:11], v[146:153], v[184:191], v[154:157]
	v_mfma_f32_16x16x128_f8f6f4 v[4:7], v[160:167], v[184:191], v[68:71]
	s_setprio 0
	s_barrier
	s_add_i32 s5, s5, 2
	s_add_u32 s40, s40, 0x100
	s_addc_u32 s41, s41, 0
	s_cmp_gt_u32 s5, 13
	s_cbranch_scc1 .LBB0_920

.LBB0_1045:
	s_add_u32 s25, s40, 0xeb800100
	v_add_u32_e32 v1, s58, v158
	s_addc_u32 s27, s41, -1
	ds_read_b128 v[136:139], v1
	ds_read_b128 v[140:143], v1 offset:1024
	ds_read_b128 v[160:163], v1 offset:2048
	ds_read_b128 v[164:167], v1 offset:3072
	v_add_u32_e32 v1, s59, v158
	s_add_u32 s44, s12, s40
	ds_read_b128 v[168:171], v1
	ds_read_b128 v[172:175], v1 offset:1024
	ds_read_b128 v[176:179], v1 offset:2048
	ds_read_b128 v[180:183], v1 offset:3072
	s_addc_u32 s45, s13, s41
	s_add_u32 s44, s44, 0xeb800100
	s_addc_u32 s45, s45, -1
	s_and_b64 s[42:43], s[42:43], exec
	s_cselect_b32 s42, s34, s44
	s_cselect_b32 s43, s35, s45
	s_cselect_b32 s27, s39, s27
	s_cselect_b32 s25, s38, s25
	s_add_u32 s44, s42, 0x80
	s_addc_u32 s45, s43, 0
	s_add_u32 s46, s90, s40
	s_addc_u32 s47, s91, s41
	s_add_u32 s46, s46, 0x80
	s_addc_u32 s47, s47, 0
	s_add_i32 m0, s1, 0xc000
	ds_read_b128 v[184:187], v151
	ds_read_b128 v[188:191], v151 offset:1024
	ds_read_b128 v[192:195], v151 offset:2048
	ds_read_b128 v[196:199], v151 offset:3072
	ds_read_b128 v[200:203], v151 offset:4096
	ds_read_b128 v[204:207], v151 offset:5120
	ds_read_b128 v[208:211], v151 offset:6144
	ds_read_b128 v[212:215], v151 offset:7168
	s_nop 0
	global_load_lds_dwordx4 v2, s[46:47]
	s_add_i32 m0, s1, 0xe000
	s_nop 0
	global_load_lds_dwordx4 v3, s[46:47]
	s_waitcnt vmcnt(8)
	s_waitcnt lgkmcnt(0)
	s_barrier
	s_setprio 1
	s_waitcnt lgkmcnt(0)
	v_mfma_f32_16x16x128_f8f6f4 v[128:131], v[136:143], v[184:191], v[128:131]
	v_mfma_f32_16x16x128_f8f6f4 v[124:127], v[160:167], v[184:191], v[124:127]
	v_mfma_f32_16x16x128_f8f6f4 v[120:123], v[136:143], v[192:199], v[120:123]
	v_mfma_f32_16x16x128_f8f6f4 v[116:119], v[160:167], v[192:199], v[116:119]
	v_mfma_f32_16x16x128_f8f6f4 v[112:115], v[136:143], v[200:207], v[112:115]
	v_mfma_f32_16x16x128_f8f6f4 v[108:111], v[160:167], v[200:207], v[108:111]
	v_mfma_f32_16x16x128_f8f6f4 v[104:107], v[136:143], v[208:215], v[104:107]
	v_mfma_f32_16x16x128_f8f6f4 v[100:103], v[160:167], v[208:215], v[100:103]
	s_setprio 0
	s_setprio 1
	v_mfma_f32_16x16x128_f8f6f4 v[144:147], v[168:175], v[184:191], v[96:99]
	v_mfma_f32_16x16x128_f8f6f4 v[184:187], v[176:183], v[184:191], v[92:95]
	v_mfma_f32_16x16x128_f8f6f4 v[188:191], v[168:175], v[192:199], v[88:91]
	v_mfma_f32_16x16x128_f8f6f4 v[192:195], v[176:183], v[192:199], v[84:87]
	v_mfma_f32_16x16x128_f8f6f4 v[196:199], v[168:175], v[200:207], v[80:83]
	v_mfma_f32_16x16x128_f8f6f4 v[200:203], v[176:183], v[200:207], v[76:79]
	v_mfma_f32_16x16x128_f8f6f4 v[204:207], v[168:175], v[208:215], v[72:75]
	v_mfma_f32_16x16x128_f8f6f4 v[208:211], v[176:183], v[208:215], v[28:31]
	s_setprio 0
	s_barrier
	s_add_i32 s64, s58, s48
	s_mov_b64 s[46:47], s[42:43]
	s_mov_b32 m0, s64
	ds_read_b128 v[68:71], v151 offset:16384
	ds_read_b128 v[72:75], v151 offset:17408
	ds_read_b128 v[76:79], v151 offset:18432
	ds_read_b128 v[80:83], v151 offset:19456
	ds_read_b128 v[84:87], v151 offset:20480
	ds_read_b128 v[88:91], v151 offset:21504
	ds_read_b128 v[92:95], v151 offset:22528
	ds_read_b128 v[96:99], v151 offset:23552
	s_nop 0
	global_load_lds_dwordx4 v148, s[46:47]
	s_add_i32 m0, s64, 0x2000
	s_nop 0
	global_load_lds_dwordx4 v150, s[46:47]
	s_add_u32 s46, s42, 0x40000
	s_addc_u32 s47, s43, 0
	s_add_i32 s64, s59, s48
	s_mov_b32 m0, s64
	s_nop 0
	global_load_lds_dwordx4 v148, s[46:47]
	s_add_i32 m0, s64, 0x2000
	s_nop 0
	global_load_lds_dwordx4 v150, s[46:47]
	s_add_u32 s46, s6, s25
	s_addc_u32 s47, s7, s27
	s_mov_b64 s[64:65], s[46:47]
	s_mov_b32 m0, s1
	s_nop 0
	global_load_lds_dwordx4 v132, s[64:65]
	s_mov_b32 m0, s11
	s_nop 0
	global_load_lds_dwordx4 v133, s[64:65]
	s_waitcnt vmcnt(8)
	s_waitcnt lgkmcnt(0)
	s_barrier
	s_setprio 1
	s_waitcnt lgkmcnt(0)
	v_mfma_f32_16x16x128_f8f6f4 v[64:67], v[136:143], v[68:75], v[64:67]
	v_mfma_f32_16x16x128_f8f6f4 v[60:63], v[160:167], v[68:75], v[60:63]
	v_mfma_f32_16x16x128_f8f6f4 v[56:59], v[136:143], v[76:83], v[56:59]
	v_mfma_f32_16x16x128_f8f6f4 v[52:55], v[160:167], v[76:83], v[52:55]
	v_mfma_f32_16x16x128_f8f6f4 v[212:215], v[136:143], v[84:91], v[48:51]
	v_mfma_f32_16x16x128_f8f6f4 v[216:219], v[160:167], v[84:91], v[44:47]
	v_mfma_f32_16x16x128_f8f6f4 v[220:223], v[136:143], v[92:99], v[40:43]
	v_mfma_f32_16x16x128_f8f6f4 v[224:227], v[160:167], v[92:99], v[36:39]
	s_setprio 0
	s_setprio 1
	v_mfma_f32_16x16x128_f8f6f4 v[232:235], v[176:183], v[68:75], v[232:235]
	v_mfma_f32_16x16x128_f8f6f4 v[228:231], v[168:175], v[68:75], v[32:35]
	v_mfma_f32_16x16x128_f8f6f4 v[236:239], v[168:175], v[76:83], v[24:27]
	v_mfma_f32_16x16x128_f8f6f4 v[240:243], v[176:183], v[76:83], v[20:23]
	v_mfma_f32_16x16x128_f8f6f4 v[244:247], v[168:175], v[84:91], v[16:19]
	v_mfma_f32_16x16x128_f8f6f4 v[248:251], v[176:183], v[84:91], v[12:15]
	v_mfma_f32_16x16x128_f8f6f4 v[154:157], v[168:175], v[92:99], v[8:11]
	v_mfma_f32_16x16x128_f8f6f4 v[68:71], v[176:183], v[92:99], v[4:7]
	s_setprio 0
	s_barrier
	s_add_i32 s25, 0, 0x18000
	v_add_u32_e32 v1, s25, v158
	s_add_i32 s27, 0, 0x1c000
	s_nop 1
	ds_read_b128 v[4:7], v1
	ds_read_b128 v[8:11], v1 offset:1024
	ds_read_b128 v[12:15], v1 offset:2048
	ds_read_b128 v[16:19], v1 offset:3072
	v_add_u32_e32 v1, s27, v158
	ds_read_b128 v[136:139], v1
	ds_read_b128 v[140:143], v1 offset:1024
	ds_read_b128 v[160:163], v1 offset:2048
	ds_read_b128 v[164:167], v1 offset:3072
	s_mov_b64 s[64:65], s[46:47]
	s_mov_b32 m0, s50
	ds_read_b128 v[20:23], v151 offset:32768
	ds_read_b128 v[24:27], v151 offset:33792
	ds_read_b128 v[28:31], v151 offset:34816
	ds_read_b128 v[32:35], v151 offset:35840
	ds_read_b128 v[36:39], v151 offset:36864
	ds_read_b128 v[40:43], v151 offset:37888
	ds_read_b128 v[44:47], v151 offset:38912
	ds_read_b128 v[48:51], v151 offset:39936
	s_nop 0
	global_load_lds_dwordx4 v134, s[64:65]
	s_mov_b32 m0, s51
	s_nop 0
	global_load_lds_dwordx4 v135, s[64:65]
	s_waitcnt vmcnt(8)
	s_waitcnt lgkmcnt(0)
	s_barrier
	s_setprio 1
	s_waitcnt lgkmcnt(0)
	v_mfma_f32_16x16x128_f8f6f4 v[128:131], v[4:11], v[20:27], v[128:131]
	v_mfma_f32_16x16x128_f8f6f4 v[124:127], v[12:19], v[20:27], v[124:127]
	v_mfma_f32_16x16x128_f8f6f4 v[120:123], v[4:11], v[28:35], v[120:123]
	v_mfma_f32_16x16x128_f8f6f4 v[116:119], v[12:19], v[28:35], v[116:119]
	v_mfma_f32_16x16x128_f8f6f4 v[112:115], v[4:11], v[36:43], v[112:115]
	v_mfma_f32_16x16x128_f8f6f4 v[108:111], v[12:19], v[36:43], v[108:111]
	v_mfma_f32_16x16x128_f8f6f4 v[104:107], v[4:11], v[44:51], v[104:107]
	v_mfma_f32_16x16x128_f8f6f4 v[100:103], v[12:19], v[44:51], v[100:103]
	s_setprio 0
	s_setprio 1
	v_mfma_f32_16x16x128_f8f6f4 v[96:99], v[136:143], v[20:27], v[144:147]
	v_mfma_f32_16x16x128_f8f6f4 v[92:95], v[160:167], v[20:27], v[184:187]
	v_mfma_f32_16x16x128_f8f6f4 v[88:91], v[136:143], v[28:35], v[188:191]
	v_mfma_f32_16x16x128_f8f6f4 v[84:87], v[160:167], v[28:35], v[192:195]
	v_mfma_f32_16x16x128_f8f6f4 v[80:83], v[136:143], v[36:43], v[196:199]
	v_mfma_f32_16x16x128_f8f6f4 v[76:79], v[160:167], v[36:43], v[200:203]
	v_mfma_f32_16x16x128_f8f6f4 v[72:75], v[136:143], v[44:51], v[204:207]
	v_mfma_f32_16x16x128_f8f6f4 v[28:31], v[160:167], v[44:51], v[208:211]
	s_setprio 0
	s_barrier
	s_add_i32 s25, s25, s48
	s_mov_b32 m0, s25
	ds_read_b128 v[20:23], v151 offset:49152
	ds_read_b128 v[24:27], v151 offset:50176
	ds_read_b128 v[168:171], v151 offset:51200
	ds_read_b128 v[172:175], v151 offset:52224
	ds_read_b128 v[176:179], v151 offset:53248
	ds_read_b128 v[180:183], v151 offset:54272
	ds_read_b128 v[184:187], v151 offset:55296
	ds_read_b128 v[188:191], v151 offset:56320
	s_nop 0
	global_load_lds_dwordx4 v148, s[44:45]
	s_add_i32 m0, s25, 0x2000
	s_add_u32 s42, s42, 0x40080
	s_addc_u32 s43, s43, 0
	s_add_i32 s25, s27, s48
	global_load_lds_dwordx4 v150, s[44:45]
	s_mov_b32 m0, s25
	s_nop 0
	global_load_lds_dwordx4 v148, s[42:43]
	s_add_i32 m0, s25, 0x2000
	s_nop 0
	global_load_lds_dwordx4 v150, s[42:43]
	s_add_u32 s42, s46, 0x80
	s_addc_u32 s43, s47, 0
	s_mov_b32 m0, s56
	s_nop 0
	global_load_lds_dwordx4 v132, s[42:43]
	s_mov_b32 m0, s57
	s_nop 0
	global_load_lds_dwordx4 v133, s[42:43]
	s_waitcnt vmcnt(8)
	s_waitcnt lgkmcnt(0)
	s_barrier
	s_setprio 1
	s_waitcnt lgkmcnt(0)
	v_mfma_f32_16x16x128_f8f6f4 v[64:67], v[4:11], v[20:27], v[64:67]
	v_mfma_f32_16x16x128_f8f6f4 v[60:63], v[12:19], v[20:27], v[60:63]
	v_mfma_f32_16x16x128_f8f6f4 v[56:59], v[4:11], v[168:175], v[56:59]
	v_mfma_f32_16x16x128_f8f6f4 v[52:55], v[12:19], v[168:175], v[52:55]
	v_mfma_f32_16x16x128_f8f6f4 v[48:51], v[4:11], v[176:183], v[212:215]
	v_mfma_f32_16x16x128_f8f6f4 v[44:47], v[12:19], v[176:183], v[216:219]
	v_mfma_f32_16x16x128_f8f6f4 v[40:43], v[4:11], v[184:191], v[220:223]
	v_mfma_f32_16x16x128_f8f6f4 v[36:39], v[12:19], v[184:191], v[224:227]
	s_setprio 0
	s_setprio 1
	v_mfma_f32_16x16x128_f8f6f4 v[32:35], v[136:143], v[20:27], v[228:231]
	v_mfma_f32_16x16x128_f8f6f4 v[232:235], v[160:167], v[20:27], v[232:235]
	v_mfma_f32_16x16x128_f8f6f4 v[24:27], v[136:143], v[168:175], v[236:239]
	v_mfma_f32_16x16x128_f8f6f4 v[20:23], v[160:167], v[168:175], v[240:243]
	v_mfma_f32_16x16x128_f8f6f4 v[16:19], v[136:143], v[176:183], v[244:247]
	v_mfma_f32_16x16x128_f8f6f4 v[12:15], v[160:167], v[176:183], v[248:251]
	v_mfma_f32_16x16x128_f8f6f4 v[8:11], v[136:143], v[184:191], v[154:157]
	v_mfma_f32_16x16x128_f8f6f4 v[4:7], v[160:167], v[184:191], v[68:71]
	s_setprio 0
	s_barrier
	s_add_i32 s23, s23, 2
	s_add_u32 s40, s40, 0x100
	s_addc_u32 s41, s41, 0
	s_cmp_gt_u32 s23, 13
	s_cbranch_scc1 .LBB0_1048
